# P6 gather: expert ids and slots of a token loaded as two 16-byte pieces up front (no per-expert load-wait round trips)
# baseline (speedup 1.0000x reference)
.LBB0_1506:
	v_lshl_add_u64 v[18:19], s[92:93], 0, v[16:17]
	s_add_u32 s12, s92, s16
	v_add_co_u32_e32 v20, vcc, 0x48200000, v18
	s_addc_u32 s13, s93, s17
	s_nop 0
	v_addc_co_u32_e32 v21, vcc, 0, v19, vcc
	global_load_dword v25, v3, s[12:13]
	v_add_co_u32_e32 v18, vcc, s20, v18
	global_load_dwordx4 v[26:29], v[20:21], off nt
	global_load_dwordx4 v[30:33], v[20:21], off offset:1024 nt
	global_load_dwordx4 v[34:37], v[20:21], off offset:2048 nt
	global_load_dwordx4 v[38:41], v[20:21], off offset:3072 nt
	v_addc_co_u32_e32 v19, vcc, 0, v19, vcc
	global_load_dwordx4 v[42:45], v[18:19], off nt
	global_load_dwordx4 v[46:49], v[18:19], off offset:1024 nt
	global_load_dwordx4 v[50:53], v[18:19], off offset:2048 nt
	global_load_dwordx4 v[54:57], v[18:19], off offset:3072 nt
	global_load_dwordx4 v[58:61], v[4:5], off
	s_ashr_i32 s11, s10, 31
	s_lshl_b64 s[12:13], s[10:11], 2
	s_add_u32 s14, s38, s12
	s_addc_u32 s15, s39, s13
	global_load_dwordx4 v[92:95], v3, s[14:15]
	global_load_dwordx4 v[62:65], v[4:5], off offset:1024
	global_load_dwordx4 v[66:69], v[4:5], off offset:2048
	global_load_dwordx4 v[70:73], v[4:5], off offset:3072
	global_load_dwordx4 v[74:77], v[8:9], off
	global_load_dwordx4 v[78:81], v[10:11], off
	global_load_dwordx4 v[82:85], v[12:13], off
	global_load_dwordx4 v[86:89], v[14:15], off
	s_add_u32 s14, s40, s12
	s_addc_u32 s15, s41, s13
	v_mov_b32_e32 v2, 0
	v_mov_b32_e32 v18, 0
	v_mov_b32_e32 v19, 0
	v_mov_b32_e32 v20, 0
	v_mov_b32_e32 v21, 0
	v_mov_b32_e32 v22, 0
	v_mov_b32_e32 v23, 0
	v_mov_b32_e32 v24, 0
	s_waitcnt vmcnt(17)
	v_mul_f32_e32 v25, 0x41000000, v25
	s_waitcnt vmcnt(16)
	v_mul_f32_e32 v26, v25, v26
	v_mul_f32_e32 v27, v25, v27
	v_mul_f32_e32 v28, v25, v28
	v_mul_f32_e32 v29, v25, v29
	s_waitcnt vmcnt(15)
	v_mul_f32_e32 v30, v25, v30
	v_mul_f32_e32 v31, v25, v31
	v_mul_f32_e32 v32, v25, v32
	v_mul_f32_e32 v33, v25, v33
	s_waitcnt vmcnt(14)
	v_mul_f32_e32 v34, v25, v34
	v_mul_f32_e32 v35, v25, v35
	v_mul_f32_e32 v36, v25, v36
	v_mul_f32_e32 v37, v25, v37
	s_waitcnt vmcnt(13)
	v_mul_f32_e32 v38, v25, v38
	v_mul_f32_e32 v39, v25, v39
	v_mul_f32_e32 v40, v25, v40
	v_mul_f32_e32 v41, v25, v41
	s_waitcnt vmcnt(12)
	v_mul_f32_e32 v42, v25, v42
	v_mul_f32_e32 v43, v25, v43
	v_mul_f32_e32 v44, v25, v44
	v_mul_f32_e32 v45, v25, v45
	s_waitcnt vmcnt(11)
	v_mul_f32_e32 v46, v25, v46
	v_mul_f32_e32 v47, v25, v47
	v_mul_f32_e32 v48, v25, v48
	v_mul_f32_e32 v49, v25, v49
	s_waitcnt vmcnt(10)
	v_mul_f32_e32 v50, v25, v50
	v_mul_f32_e32 v51, v25, v51
	v_mul_f32_e32 v52, v25, v52
	v_mul_f32_e32 v53, v25, v53
	s_waitcnt vmcnt(9)
	v_mul_f32_e32 v54, v25, v54
	v_mul_f32_e32 v55, v25, v55
	v_mul_f32_e32 v56, v25, v56
	v_mul_f32_e32 v25, v25, v57
	s_waitcnt vmcnt(7)
	v_lshlrev_b32_e32 v57, 2, v92
	v_add_u32_e32 v57, 0, v57
	v_add_u32_e32 v57, 0x20400, v57
	v_mul_f32_e32 v26, v26, v58
	ds_read_b32 v57, v57
	global_load_dwordx4 v[96:99], v3, s[14:15]
	v_mul_f32_e32 v27, v27, v59
	s_waitcnt vmcnt(7)
	v_mul_f32_e32 v30, v30, v62
	v_mul_f32_e32 v31, v31, v63
	s_waitcnt vmcnt(6)
	v_mul_f32_e32 v34, v34, v66
	v_mul_f32_e32 v35, v35, v67
	s_waitcnt vmcnt(5)
	v_mul_f32_e32 v38, v38, v70
	v_mul_f32_e32 v39, v39, v71
	s_waitcnt vmcnt(4)
	v_mul_f32_e32 v42, v42, v74
	v_mul_f32_e32 v43, v43, v75
	s_waitcnt vmcnt(3)
	v_mul_f32_e32 v46, v46, v78
	v_mul_f32_e32 v47, v47, v79
	s_waitcnt vmcnt(2)
	v_mul_f32_e32 v50, v50, v82
	v_mul_f32_e32 v51, v51, v83
	s_waitcnt vmcnt(1)
	v_mul_f32_e32 v54, v54, v86
	v_mul_f32_e32 v55, v55, v87
	v_med3_f32 v26, v26, s19, v1
	v_med3_f32 v27, v27, s19, v1
	v_med3_f32 v30, v30, s19, v1
	v_med3_f32 v31, v31, s19, v1
	v_med3_f32 v34, v34, s19, v1
	v_med3_f32 v35, v35, s19, v1
	v_med3_f32 v38, v38, s19, v1
	v_med3_f32 v39, v39, s19, v1
	v_med3_f32 v42, v42, s19, v1
	v_med3_f32 v43, v43, s19, v1
	v_med3_f32 v46, v46, s19, v1
	v_med3_f32 v47, v47, s19, v1
	v_med3_f32 v50, v50, s19, v1
	v_med3_f32 v51, v51, s19, v1
	v_med3_f32 v54, v54, s19, v1
	v_med3_f32 v55, v55, s19, v1
	v_cvt_pk_fp8_f32 v2, v26, v27
	v_cvt_pk_fp8_f32 v18, v30, v31
	v_cvt_pk_fp8_f32 v19, v34, v35
	v_cvt_pk_fp8_f32 v20, v38, v39
	v_cvt_pk_fp8_f32 v21, v42, v43
	v_cvt_pk_fp8_f32 v22, v46, v47
	v_cvt_pk_fp8_f32 v23, v50, v51
	v_cvt_pk_fp8_f32 v24, v54, v55
	v_mul_f32_e32 v28, v28, v60
	v_mul_f32_e32 v29, v29, v61
	v_mul_f32_e32 v32, v32, v64
	v_mul_f32_e32 v33, v33, v65
	v_mul_f32_e32 v36, v36, v68
	v_mul_f32_e32 v37, v37, v69
	v_mul_f32_e32 v40, v40, v72
	v_mul_f32_e32 v41, v41, v73
	v_mul_f32_e32 v44, v44, v76
	v_mul_f32_e32 v45, v45, v77
	v_mul_f32_e32 v48, v48, v80
	v_mul_f32_e32 v49, v49, v81
	v_mul_f32_e32 v52, v52, v84
	v_mul_f32_e32 v53, v53, v85
	v_mul_f32_e32 v56, v56, v88
	v_mul_f32_e32 v25, v25, v89
	v_med3_f32 v28, v28, s19, v1
	v_med3_f32 v29, v29, s19, v1
	v_med3_f32 v32, v32, s19, v1
	v_med3_f32 v33, v33, s19, v1
	v_med3_f32 v36, v36, s19, v1
	v_med3_f32 v37, v37, s19, v1
	v_med3_f32 v40, v40, s19, v1
	v_med3_f32 v41, v41, s19, v1
	v_med3_f32 v44, v44, s19, v1
	v_med3_f32 v45, v45, s19, v1
	v_med3_f32 v48, v48, s19, v1
	v_med3_f32 v49, v49, s19, v1
	v_med3_f32 v52, v52, s19, v1
	v_med3_f32 v53, v53, s19, v1
	v_med3_f32 v56, v56, s19, v1
	v_med3_f32 v25, v25, s19, v1
	v_cvt_pk_fp8_f32 v2, v28, v29 op_sel:[0,0,1]
	v_cvt_pk_fp8_f32 v18, v32, v33 op_sel:[0,0,1]
	v_cvt_pk_fp8_f32 v19, v36, v37 op_sel:[0,0,1]
	v_cvt_pk_fp8_f32 v20, v40, v41 op_sel:[0,0,1]
	v_cvt_pk_fp8_f32 v21, v44, v45 op_sel:[0,0,1]
	v_cvt_pk_fp8_f32 v22, v48, v49 op_sel:[0,0,1]
	v_cvt_pk_fp8_f32 v23, v52, v53 op_sel:[0,0,1]
	v_cvt_pk_fp8_f32 v24, v56, v25 op_sel:[0,0,1]
	s_waitcnt lgkmcnt(0)
	v_lshlrev_b32_e32 v25, 8, v57
	s_waitcnt vmcnt(0)
	v_add_u32_e32 v25, v25, v96
	v_mad_i64_i32 v[26:27], s[14:15], v25, s21, v[6:7]
	global_store_dword v[26:27], v2, off nt
	global_store_dword v[26:27], v18, off offset:256 nt
	global_store_dword v[26:27], v19, off offset:512 nt
	global_store_dword v[26:27], v20, off offset:768 nt
	global_store_dword v[26:27], v21, off offset:1024 nt
	global_store_dword v[26:27], v22, off offset:1280 nt
	global_store_dword v[26:27], v23, off offset:1536 nt
	global_store_dword v[26:27], v24, off offset:1792 nt
	s_and_saveexec_b64 s[14:15], s[2:3]
	s_cbranch_execz .LBB0_1508
	s_add_u32 s12, s33, s12
	s_addc_u32 s13, s42, s13
	global_store_dword v3, v25, s[12:13]
.LBB0_1508:
	s_or_b64 exec, exec, s[14:15]
	s_add_i32 s12, s10, 1
	s_ashr_i32 s13, s12, 31
	s_lshl_b64 s[12:13], s[12:13], 2
	s_add_u32 s14, s38, s12
	s_addc_u32 s15, s39, s13
	v_lshlrev_b32_e32 v25, 2, v93
	s_add_u32 s14, s40, s12
	s_addc_u32 s15, s41, s13
	v_add_u32_e32 v25, 0, v25
	v_add_u32_e32 v25, 0x20400, v25
	ds_read_b32 v25, v25
	s_waitcnt lgkmcnt(0)
	v_lshlrev_b32_e32 v25, 8, v25
	v_add_u32_e32 v25, v25, v97
	v_mad_i64_i32 v[26:27], s[14:15], v25, s21, v[6:7]
	global_store_dword v[26:27], v2, off nt
	global_store_dword v[26:27], v18, off offset:256 nt
	global_store_dword v[26:27], v19, off offset:512 nt
	global_store_dword v[26:27], v20, off offset:768 nt
	global_store_dword v[26:27], v21, off offset:1024 nt
	global_store_dword v[26:27], v22, off offset:1280 nt
	global_store_dword v[26:27], v23, off offset:1536 nt
	global_store_dword v[26:27], v24, off offset:1792 nt
	s_and_saveexec_b64 s[14:15], s[2:3]
	s_cbranch_execz .LBB0_1510
	s_add_u32 s12, s33, s12
	s_addc_u32 s13, s42, s13
	global_store_dword v3, v25, s[12:13]
.LBB0_1510:
	s_or_b64 exec, exec, s[14:15]
	s_add_i32 s12, s10, 2
	s_ashr_i32 s13, s12, 31
	s_lshl_b64 s[12:13], s[12:13], 2
	s_add_u32 s14, s38, s12
	s_addc_u32 s15, s39, s13
	v_lshlrev_b32_e32 v25, 2, v94
	s_add_u32 s14, s40, s12
	s_addc_u32 s15, s41, s13
	v_add_u32_e32 v25, 0, v25
	v_add_u32_e32 v25, 0x20400, v25
	ds_read_b32 v25, v25
	s_waitcnt lgkmcnt(0)
	v_lshlrev_b32_e32 v25, 8, v25
	v_add_u32_e32 v25, v25, v98
	v_mad_i64_i32 v[26:27], s[14:15], v25, s21, v[6:7]
	global_store_dword v[26:27], v2, off nt
	global_store_dword v[26:27], v18, off offset:256 nt
	global_store_dword v[26:27], v19, off offset:512 nt
	global_store_dword v[26:27], v20, off offset:768 nt
	global_store_dword v[26:27], v21, off offset:1024 nt
	global_store_dword v[26:27], v22, off offset:1280 nt
	global_store_dword v[26:27], v23, off offset:1536 nt
	global_store_dword v[26:27], v24, off offset:1792 nt
	s_and_saveexec_b64 s[14:15], s[2:3]
	s_cbranch_execz .LBB0_1512
	s_add_u32 s12, s33, s12
	s_addc_u32 s13, s42, s13
	global_store_dword v3, v25, s[12:13]
.LBB0_1512:
	s_or_b64 exec, exec, s[14:15]
	s_add_i32 s12, s10, 3
	s_ashr_i32 s13, s12, 31
	s_lshl_b64 s[12:13], s[12:13], 2
	s_add_u32 s14, s38, s12
	s_addc_u32 s15, s39, s13
	v_lshlrev_b32_e32 v25, 2, v95
	s_add_u32 s14, s40, s12
	s_addc_u32 s15, s41, s13
	v_add_u32_e32 v25, 0, v25
	v_add_u32_e32 v25, 0x20400, v25
	ds_read_b32 v25, v25
	s_waitcnt lgkmcnt(0)
	v_lshlrev_b32_e32 v25, 8, v25
	v_add_u32_e32 v25, v25, v99
	v_mad_i64_i32 v[26:27], s[14:15], v25, s21, v[6:7]
	global_store_dword v[26:27], v2, off nt
	global_store_dword v[26:27], v18, off offset:256 nt
	global_store_dword v[26:27], v19, off offset:512 nt
	global_store_dword v[26:27], v20, off offset:768 nt
	global_store_dword v[26:27], v21, off offset:1024 nt
	global_store_dword v[26:27], v22, off offset:1280 nt
	global_store_dword v[26:27], v23, off offset:1536 nt
	global_store_dword v[26:27], v24, off offset:1792 nt
	s_and_saveexec_b64 s[14:15], s[2:3]
	s_cbranch_execz .LBB0_1505
	s_add_u32 s12, s33, s12
	s_addc_u32 s13, s42, s13
	global_store_dword v3, v25, s[12:13]
	s_branch .LBB0_1505
